# prologue: X f32->bf16 copy loop 8 loads deep, sc staging loads hoisted, adaLN loop unrolled (on top of attention LDS pipelining)
# speedup vs baseline: 1.0019x; 1.0019x over previous
.LBB0_79:
	s_mov_b32 s3, 0
	s_lshl_b64 s[4:5], s[2:3], 9
	v_ashrrev_i32_e32 v171, 31, v170
	s_ashr_i32 s35, s34, 31
	v_lshl_add_u64 v[2:3], s[4:5], 0, v[170:171]
	s_mov_b64 s[4:5], 0x440000
	s_lshl_b64 s[12:13], s[34:35], 9
	s_mov_b32 s8, 2
	s_mov_b32 s6, s3
	v_cmp_gt_u64_e32 vcc, s[4:5], v[2:3]
	s_and_saveexec_b64 s[4:5], vcc
	s_cbranch_execz .LBB0_82
	s_ashr_i32 s9, s8, 31
	s_lshl_b64 s[8:9], s[8:9], 3
	s_add_u32 s8, s0, s8
	s_addc_u32 s9, s1, s9
	s_ashr_i32 s7, s6, 31
	s_lshl_b64 s[6:7], s[6:7], 3
	s_add_u32 s14, s0, s6
	s_addc_u32 s15, s1, s7
	s_load_dwordx2 s[6:7], s[8:9], 0x0
	s_load_dwordx2 s[16:17], s[14:15], 0x0
	s_lshl_b64 s[8:9], s[2:3], 12
	s_add_u32 s8, s26, s8
	s_addc_u32 s9, s27, s9
	v_lshl_add_u64 v[4:5], v[170:171], 3, s[8:9]
	s_mov_b64 s[8:9], 0x1b700000
	v_lshl_add_u64 v[4:5], v[4:5], 0, s[8:9]
	s_lshl_b64 s[8:9], s[34:35], 12
	s_waitcnt lgkmcnt(0)
	s_add_u32 s14, s16, 0xffc00000
	s_addc_u32 s15, s17, -1
	s_lshl_b64 s[16:17], s[2:3], 13
	v_lshl_add_u64 v[6:7], v[170:171], 4, s[16:17]
	s_lshl_b64 s[16:17], s[34:35], 13
	s_mov_b64 s[18:19], 0
	s_mov_b64 s[20:21], 0x40000
	s_movk_i32 s28, 0x7fff
	s_mov_b32 s29, 0xffff0000
	s_mov_b64 s[22:23], 0x43ffff
	v_mov_b64_e32 v[8:9], v[2:3]
	s_cmp_eq_u64 exec, -1
	s_cbranch_scc0 .Lmy_xcp_tail
	s_lshl_b32 s99, s12, 3
	s_mov_b32 s98, s99
.Lmy_xcp_loop:
	s_cmp_le_u32 s98, 0x440000
	s_cbranch_scc0 .Lmy_xcp_tail
	v_lshl_add_u64 v[226:227], s[6:7], 0, v[6:7]
	v_lshl_add_u64 v[228:229], s[14:15], 0, v[6:7]
	v_cmp_gt_u64_e32 vcc, s[20:21], v[8:9]
	v_lshl_add_u64 v[8:9], v[8:9], 0, s[12:13]
	v_lshl_add_u64 v[6:7], v[6:7], 0, s[16:17]
	v_cndmask_b32_e32 v227, v229, v227, vcc
	v_cndmask_b32_e32 v226, v228, v226, vcc
	global_load_dwordx4 v[192:195], v[226:227], off
	v_lshl_add_u64 v[226:227], s[6:7], 0, v[6:7]
	v_lshl_add_u64 v[228:229], s[14:15], 0, v[6:7]
	v_cmp_gt_u64_e32 vcc, s[20:21], v[8:9]
	v_lshl_add_u64 v[8:9], v[8:9], 0, s[12:13]
	v_lshl_add_u64 v[6:7], v[6:7], 0, s[16:17]
	v_cndmask_b32_e32 v227, v229, v227, vcc
	v_cndmask_b32_e32 v226, v228, v226, vcc
	global_load_dwordx4 v[196:199], v[226:227], off
	v_lshl_add_u64 v[226:227], s[6:7], 0, v[6:7]
	v_lshl_add_u64 v[228:229], s[14:15], 0, v[6:7]
	v_cmp_gt_u64_e32 vcc, s[20:21], v[8:9]
	v_lshl_add_u64 v[8:9], v[8:9], 0, s[12:13]
	v_lshl_add_u64 v[6:7], v[6:7], 0, s[16:17]
	v_cndmask_b32_e32 v227, v229, v227, vcc
	v_cndmask_b32_e32 v226, v228, v226, vcc
	global_load_dwordx4 v[200:203], v[226:227], off
	v_lshl_add_u64 v[226:227], s[6:7], 0, v[6:7]
	v_lshl_add_u64 v[228:229], s[14:15], 0, v[6:7]
	v_cmp_gt_u64_e32 vcc, s[20:21], v[8:9]
	v_lshl_add_u64 v[8:9], v[8:9], 0, s[12:13]
	v_lshl_add_u64 v[6:7], v[6:7], 0, s[16:17]
	v_cndmask_b32_e32 v227, v229, v227, vcc
	v_cndmask_b32_e32 v226, v228, v226, vcc
	global_load_dwordx4 v[204:207], v[226:227], off
	v_lshl_add_u64 v[226:227], s[6:7], 0, v[6:7]
	v_lshl_add_u64 v[228:229], s[14:15], 0, v[6:7]
	v_cmp_gt_u64_e32 vcc, s[20:21], v[8:9]
	v_lshl_add_u64 v[8:9], v[8:9], 0, s[12:13]
	v_lshl_add_u64 v[6:7], v[6:7], 0, s[16:17]
	v_cndmask_b32_e32 v227, v229, v227, vcc
	v_cndmask_b32_e32 v226, v228, v226, vcc
	global_load_dwordx4 v[208:211], v[226:227], off
	v_lshl_add_u64 v[226:227], s[6:7], 0, v[6:7]
	v_lshl_add_u64 v[228:229], s[14:15], 0, v[6:7]
	v_cmp_gt_u64_e32 vcc, s[20:21], v[8:9]
	v_lshl_add_u64 v[8:9], v[8:9], 0, s[12:13]
	v_lshl_add_u64 v[6:7], v[6:7], 0, s[16:17]
	v_cndmask_b32_e32 v227, v229, v227, vcc
	v_cndmask_b32_e32 v226, v228, v226, vcc
	global_load_dwordx4 v[212:215], v[226:227], off
	v_lshl_add_u64 v[226:227], s[6:7], 0, v[6:7]
	v_lshl_add_u64 v[228:229], s[14:15], 0, v[6:7]
	v_cmp_gt_u64_e32 vcc, s[20:21], v[8:9]
	v_lshl_add_u64 v[8:9], v[8:9], 0, s[12:13]
	v_lshl_add_u64 v[6:7], v[6:7], 0, s[16:17]
	v_cndmask_b32_e32 v227, v229, v227, vcc
	v_cndmask_b32_e32 v226, v228, v226, vcc
	global_load_dwordx4 v[216:219], v[226:227], off
	v_lshl_add_u64 v[226:227], s[6:7], 0, v[6:7]
	v_lshl_add_u64 v[228:229], s[14:15], 0, v[6:7]
	v_cmp_gt_u64_e32 vcc, s[20:21], v[8:9]
	v_lshl_add_u64 v[8:9], v[8:9], 0, s[12:13]
	v_lshl_add_u64 v[6:7], v[6:7], 0, s[16:17]
	v_cndmask_b32_e32 v227, v229, v227, vcc
	v_cndmask_b32_e32 v226, v228, v226, vcc
	global_load_dwordx4 v[220:223], v[226:227], off
	s_waitcnt vmcnt(7)
	v_bfe_u32 v1, v192, 16, 1
	v_bfe_u32 v14, v193, 16, 1
	v_bfe_u32 v15, v194, 16, 1
	v_bfe_u32 v16, v195, 16, 1
	v_add3_u32 v1, v192, v1, s28
	v_add3_u32 v10, v193, v14, s28
	v_add3_u32 v11, v194, v15, s28
	v_add3_u32 v12, v195, v16, s28
	v_lshrrev_b32_e32 v1, 16, v1
	v_lshrrev_b32_e32 v11, 16, v11
	v_and_or_b32 v10, v10, s29, v1
	v_and_or_b32 v11, v12, s29, v11
	global_store_dwordx2 v[4:5], v[10:11], off
	v_lshl_add_u64 v[4:5], v[4:5], 0, s[8:9]
	s_waitcnt vmcnt(7)
	v_bfe_u32 v1, v196, 16, 1
	v_bfe_u32 v14, v197, 16, 1
	v_bfe_u32 v15, v198, 16, 1
	v_bfe_u32 v16, v199, 16, 1
	v_add3_u32 v1, v196, v1, s28
	v_add3_u32 v10, v197, v14, s28
	v_add3_u32 v11, v198, v15, s28
	v_add3_u32 v12, v199, v16, s28
	v_lshrrev_b32_e32 v1, 16, v1
	v_lshrrev_b32_e32 v11, 16, v11
	v_and_or_b32 v10, v10, s29, v1
	v_and_or_b32 v11, v12, s29, v11
	global_store_dwordx2 v[4:5], v[10:11], off
	v_lshl_add_u64 v[4:5], v[4:5], 0, s[8:9]
	s_waitcnt vmcnt(7)
	v_bfe_u32 v1, v200, 16, 1
	v_bfe_u32 v14, v201, 16, 1
	v_bfe_u32 v15, v202, 16, 1
	v_bfe_u32 v16, v203, 16, 1
	v_add3_u32 v1, v200, v1, s28
	v_add3_u32 v10, v201, v14, s28
	v_add3_u32 v11, v202, v15, s28
	v_add3_u32 v12, v203, v16, s28
	v_lshrrev_b32_e32 v1, 16, v1
	v_lshrrev_b32_e32 v11, 16, v11
	v_and_or_b32 v10, v10, s29, v1
	v_and_or_b32 v11, v12, s29, v11
	global_store_dwordx2 v[4:5], v[10:11], off
	v_lshl_add_u64 v[4:5], v[4:5], 0, s[8:9]
	s_waitcnt vmcnt(7)
	v_bfe_u32 v1, v204, 16, 1
	v_bfe_u32 v14, v205, 16, 1
	v_bfe_u32 v15, v206, 16, 1
	v_bfe_u32 v16, v207, 16, 1
	v_add3_u32 v1, v204, v1, s28
	v_add3_u32 v10, v205, v14, s28
	v_add3_u32 v11, v206, v15, s28
	v_add3_u32 v12, v207, v16, s28
	v_lshrrev_b32_e32 v1, 16, v1
	v_lshrrev_b32_e32 v11, 16, v11
	v_and_or_b32 v10, v10, s29, v1
	v_and_or_b32 v11, v12, s29, v11
	global_store_dwordx2 v[4:5], v[10:11], off
	v_lshl_add_u64 v[4:5], v[4:5], 0, s[8:9]
	s_waitcnt vmcnt(7)
	v_bfe_u32 v1, v208, 16, 1
	v_bfe_u32 v14, v209, 16, 1
	v_bfe_u32 v15, v210, 16, 1
	v_bfe_u32 v16, v211, 16, 1
	v_add3_u32 v1, v208, v1, s28
	v_add3_u32 v10, v209, v14, s28
	v_add3_u32 v11, v210, v15, s28
	v_add3_u32 v12, v211, v16, s28
	v_lshrrev_b32_e32 v1, 16, v1
	v_lshrrev_b32_e32 v11, 16, v11
	v_and_or_b32 v10, v10, s29, v1
	v_and_or_b32 v11, v12, s29, v11
	global_store_dwordx2 v[4:5], v[10:11], off
	v_lshl_add_u64 v[4:5], v[4:5], 0, s[8:9]
	s_waitcnt vmcnt(7)
	v_bfe_u32 v1, v212, 16, 1
	v_bfe_u32 v14, v213, 16, 1
	v_bfe_u32 v15, v214, 16, 1
	v_bfe_u32 v16, v215, 16, 1
	v_add3_u32 v1, v212, v1, s28
	v_add3_u32 v10, v213, v14, s28
	v_add3_u32 v11, v214, v15, s28
	v_add3_u32 v12, v215, v16, s28
	v_lshrrev_b32_e32 v1, 16, v1
	v_lshrrev_b32_e32 v11, 16, v11
	v_and_or_b32 v10, v10, s29, v1
	v_and_or_b32 v11, v12, s29, v11
	global_store_dwordx2 v[4:5], v[10:11], off
	v_lshl_add_u64 v[4:5], v[4:5], 0, s[8:9]
	s_waitcnt vmcnt(7)
	v_bfe_u32 v1, v216, 16, 1
	v_bfe_u32 v14, v217, 16, 1
	v_bfe_u32 v15, v218, 16, 1
	v_bfe_u32 v16, v219, 16, 1
	v_add3_u32 v1, v216, v1, s28
	v_add3_u32 v10, v217, v14, s28
	v_add3_u32 v11, v218, v15, s28
	v_add3_u32 v12, v219, v16, s28
	v_lshrrev_b32_e32 v1, 16, v1
	v_lshrrev_b32_e32 v11, 16, v11
	v_and_or_b32 v10, v10, s29, v1
	v_and_or_b32 v11, v12, s29, v11
	global_store_dwordx2 v[4:5], v[10:11], off
	v_lshl_add_u64 v[4:5], v[4:5], 0, s[8:9]
	s_waitcnt vmcnt(7)
	v_bfe_u32 v1, v220, 16, 1
	v_bfe_u32 v14, v221, 16, 1
	v_bfe_u32 v15, v222, 16, 1
	v_bfe_u32 v16, v223, 16, 1
	v_add3_u32 v1, v220, v1, s28
	v_add3_u32 v10, v221, v14, s28
	v_add3_u32 v11, v222, v15, s28
	v_add3_u32 v12, v223, v16, s28
	v_lshrrev_b32_e32 v1, 16, v1
	v_lshrrev_b32_e32 v11, 16, v11
	v_and_or_b32 v10, v10, s29, v1
	v_and_or_b32 v11, v12, s29, v11
	global_store_dwordx2 v[4:5], v[10:11], off
	v_lshl_add_u64 v[4:5], v[4:5], 0, s[8:9]
	s_add_u32 s98, s98, s99
	s_branch .Lmy_xcp_loop
.Lmy_xcp_tail:
	v_cmp_ge_u64_e32 vcc, s[22:23], v[8:9]
	s_and_b64 exec, exec, vcc
	s_cbranch_execz .LBB0_82

.LBB0_108:
	s_or_b64 exec, exec, s[14:15]
	s_movk_i32 s3, 0x1400
	v_cmp_gt_i32_e32 vcc, s3, v170
	s_barrier
	s_and_saveexec_b64 s[4:5], vcc
	s_cbranch_execz .LBB0_115
	s_load_dwordx2 s[16:17], s[0:1], 0x8
	s_load_dwordx2 s[6:7], s[0:1], 0x18
	v_lshlrev_b32_e32 v1, 2, v170
	s_waitcnt lgkmcnt(0)
	s_add_u32 s8, s16, 0x1000
	s_addc_u32 s9, s17, 0
	s_add_u32 s12, s16, 0x2000
	s_addc_u32 s13, s17, 0
	s_add_u32 s14, s16, 0x3000
	s_addc_u32 s15, s17, 0
	global_load_dword v192, v1, s[16:17]
	global_load_dword v193, v1, s[16:17] offset:2048
	global_load_dword v194, v1, s[8:9]
	global_load_dword v195, v1, s[8:9] offset:2048
	global_load_dword v196, v1, s[12:13]
	global_load_dword v197, v1, s[12:13] offset:2048
	global_load_dword v198, v1, s[14:15]
	global_load_dword v199, v1, s[14:15] offset:2048
	global_load_dword v200, v1, s[6:7]
	global_load_dword v201, v1, s[6:7] offset:2048
	s_waitcnt vmcnt(9)
	v_mul_f32_e32 v6, 0xbfb8aa3b, v192
	v_exp_f32_e32 v6, v6
	s_nop 0
	v_add_f32_e32 v6, 1.0, v6
	v_div_scale_f32 v8, s[18:19], v6, v6, 1.0
	v_rcp_f32_e32 v9, v8
	v_div_scale_f32 v10, vcc, 1.0, v6, 1.0
	v_fma_f32 v11, -v8, v9, 1.0
	v_fmac_f32_e32 v9, v11, v9
	v_mul_f32_e32 v11, v10, v9
	v_fma_f32 v12, -v8, v11, v10
	v_fmac_f32_e32 v11, v12, v9
	v_fma_f32 v8, -v8, v11, v10
	v_div_fmas_f32 v8, v8, v9, v11
	v_div_fixup_f32 v6, v8, v6, 1.0
	v_mul_f32_e32 v192, v192, v6
	ds_write_b32 v1, v192
	s_waitcnt vmcnt(8)
	v_mul_f32_e32 v6, 0xbfb8aa3b, v193
	v_exp_f32_e32 v6, v6
	s_nop 0
	v_add_f32_e32 v6, 1.0, v6
	v_div_scale_f32 v8, s[18:19], v6, v6, 1.0
	v_rcp_f32_e32 v9, v8
	v_div_scale_f32 v10, vcc, 1.0, v6, 1.0
	v_fma_f32 v11, -v8, v9, 1.0
	v_fmac_f32_e32 v9, v11, v9
	v_mul_f32_e32 v11, v10, v9
	v_fma_f32 v12, -v8, v11, v10
	v_fmac_f32_e32 v11, v12, v9
	v_fma_f32 v8, -v8, v11, v10
	v_div_fmas_f32 v8, v8, v9, v11
	v_div_fixup_f32 v6, v8, v6, 1.0
	v_mul_f32_e32 v193, v193, v6
	ds_write_b32 v1, v193 offset:2048
	s_waitcnt vmcnt(7)
	v_mul_f32_e32 v6, 0xbfb8aa3b, v194
	v_exp_f32_e32 v6, v6
	s_nop 0
	v_add_f32_e32 v6, 1.0, v6
	v_div_scale_f32 v8, s[18:19], v6, v6, 1.0
	v_rcp_f32_e32 v9, v8
	v_div_scale_f32 v10, vcc, 1.0, v6, 1.0
	v_fma_f32 v11, -v8, v9, 1.0
	v_fmac_f32_e32 v9, v11, v9
	v_mul_f32_e32 v11, v10, v9
	v_fma_f32 v12, -v8, v11, v10
	v_fmac_f32_e32 v11, v12, v9
	v_fma_f32 v8, -v8, v11, v10
	v_div_fmas_f32 v8, v8, v9, v11
	v_div_fixup_f32 v6, v8, v6, 1.0
	v_mul_f32_e32 v194, v194, v6
	ds_write_b32 v1, v194 offset:4096
	s_waitcnt vmcnt(6)
	v_mul_f32_e32 v6, 0xbfb8aa3b, v195
	v_exp_f32_e32 v6, v6
	s_nop 0
	v_add_f32_e32 v6, 1.0, v6
	v_div_scale_f32 v8, s[18:19], v6, v6, 1.0
	v_rcp_f32_e32 v9, v8
	v_div_scale_f32 v10, vcc, 1.0, v6, 1.0
	v_fma_f32 v11, -v8, v9, 1.0
	v_fmac_f32_e32 v9, v11, v9
	v_mul_f32_e32 v11, v10, v9
	v_fma_f32 v12, -v8, v11, v10
	v_fmac_f32_e32 v11, v12, v9
	v_fma_f32 v8, -v8, v11, v10
	v_div_fmas_f32 v8, v8, v9, v11
	v_div_fixup_f32 v6, v8, v6, 1.0
	v_mul_f32_e32 v195, v195, v6
	ds_write_b32 v1, v195 offset:6144
	s_waitcnt vmcnt(5)
	v_mul_f32_e32 v6, 0xbfb8aa3b, v196
	v_exp_f32_e32 v6, v6
	s_nop 0
	v_add_f32_e32 v6, 1.0, v6
	v_div_scale_f32 v8, s[18:19], v6, v6, 1.0
	v_rcp_f32_e32 v9, v8
	v_div_scale_f32 v10, vcc, 1.0, v6, 1.0
	v_fma_f32 v11, -v8, v9, 1.0
	v_fmac_f32_e32 v9, v11, v9
	v_mul_f32_e32 v11, v10, v9
	v_fma_f32 v12, -v8, v11, v10
	v_fmac_f32_e32 v11, v12, v9
	v_fma_f32 v8, -v8, v11, v10
	v_div_fmas_f32 v8, v8, v9, v11
	v_div_fixup_f32 v6, v8, v6, 1.0
	v_mul_f32_e32 v196, v196, v6
	ds_write_b32 v1, v196 offset:8192
	s_waitcnt vmcnt(4)
	v_mul_f32_e32 v6, 0xbfb8aa3b, v197
	v_exp_f32_e32 v6, v6
	s_nop 0
	v_add_f32_e32 v6, 1.0, v6
	v_div_scale_f32 v8, s[18:19], v6, v6, 1.0
	v_rcp_f32_e32 v9, v8
	v_div_scale_f32 v10, vcc, 1.0, v6, 1.0
	v_fma_f32 v11, -v8, v9, 1.0
	v_fmac_f32_e32 v9, v11, v9
	v_mul_f32_e32 v11, v10, v9
	v_fma_f32 v12, -v8, v11, v10
	v_fmac_f32_e32 v11, v12, v9
	v_fma_f32 v8, -v8, v11, v10
	v_div_fmas_f32 v8, v8, v9, v11
	v_div_fixup_f32 v6, v8, v6, 1.0
	v_mul_f32_e32 v197, v197, v6
	ds_write_b32 v1, v197 offset:10240
	s_waitcnt vmcnt(3)
	v_mul_f32_e32 v6, 0xbfb8aa3b, v198
	v_exp_f32_e32 v6, v6
	s_nop 0
	v_add_f32_e32 v6, 1.0, v6
	v_div_scale_f32 v8, s[18:19], v6, v6, 1.0
	v_rcp_f32_e32 v9, v8
	v_div_scale_f32 v10, vcc, 1.0, v6, 1.0
	v_fma_f32 v11, -v8, v9, 1.0
	v_fmac_f32_e32 v9, v11, v9
	v_mul_f32_e32 v11, v10, v9
	v_fma_f32 v12, -v8, v11, v10
	v_fmac_f32_e32 v11, v12, v9
	v_fma_f32 v8, -v8, v11, v10
	v_div_fmas_f32 v8, v8, v9, v11
	v_div_fixup_f32 v6, v8, v6, 1.0
	v_mul_f32_e32 v198, v198, v6
	ds_write_b32 v1, v198 offset:12288
	s_waitcnt vmcnt(2)
	v_mul_f32_e32 v6, 0xbfb8aa3b, v199
	v_exp_f32_e32 v6, v6
	s_nop 0
	v_add_f32_e32 v6, 1.0, v6
	v_div_scale_f32 v8, s[18:19], v6, v6, 1.0
	v_rcp_f32_e32 v9, v8
	v_div_scale_f32 v10, vcc, 1.0, v6, 1.0
	v_fma_f32 v11, -v8, v9, 1.0
	v_fmac_f32_e32 v9, v11, v9
	v_mul_f32_e32 v11, v10, v9
	v_fma_f32 v12, -v8, v11, v10
	v_fmac_f32_e32 v11, v12, v9
	v_fma_f32 v8, -v8, v11, v10
	v_div_fmas_f32 v8, v8, v9, v11
	v_div_fixup_f32 v6, v8, v6, 1.0
	v_mul_f32_e32 v199, v199, v6
	ds_write_b32 v1, v199 offset:14336
	s_waitcnt vmcnt(1)
	v_mul_f32_e32 v6, 0xbfb8aa3b, v200
	v_exp_f32_e32 v6, v6
	s_nop 0
	v_add_f32_e32 v6, 1.0, v6
	v_div_scale_f32 v8, s[18:19], v6, v6, 1.0
	v_rcp_f32_e32 v9, v8
	v_div_scale_f32 v10, vcc, 1.0, v6, 1.0
	v_fma_f32 v11, -v8, v9, 1.0
	v_fmac_f32_e32 v9, v11, v9
	v_mul_f32_e32 v11, v10, v9
	v_fma_f32 v12, -v8, v11, v10
	v_fmac_f32_e32 v11, v12, v9
	v_fma_f32 v8, -v8, v11, v10
	v_div_fmas_f32 v8, v8, v9, v11
	v_div_fixup_f32 v6, v8, v6, 1.0
	v_mul_f32_e32 v200, v200, v6
	ds_write_b32 v1, v200 offset:16384
	s_waitcnt vmcnt(0)
	v_mul_f32_e32 v6, 0xbfb8aa3b, v201
	v_exp_f32_e32 v6, v6
	s_nop 0
	v_add_f32_e32 v6, 1.0, v6
	v_div_scale_f32 v8, s[18:19], v6, v6, 1.0
	v_rcp_f32_e32 v9, v8
	v_div_scale_f32 v10, vcc, 1.0, v6, 1.0
	v_fma_f32 v11, -v8, v9, 1.0
	v_fmac_f32_e32 v9, v11, v9
	v_mul_f32_e32 v11, v10, v9
	v_fma_f32 v12, -v8, v11, v10
	v_fmac_f32_e32 v11, v12, v9
	v_fma_f32 v8, -v8, v11, v10
	v_div_fmas_f32 v8, v8, v9, v11
	v_div_fixup_f32 v6, v8, v6, 1.0
	v_mul_f32_e32 v201, v201, v6
	ds_write_b32 v1, v201 offset:18432
